# layer-0 GLA even chunks: state-update k_end^T fragments run four MFMAs ahead (four quads) and v fragments double-buffered in idle registers with counted lgkmcnt waits (was one LDS round trip per MFMA)
# baseline (speedup 1.0000x reference)
; #define LAS __attribute__((address_space(3)))
; __device__ __forceinline__ void gla_unit(LAS unsigned char* lds, const unsigned char* ws, const float* g_onorm, const int b, const int h, const int wv) {
;     ...
;         f32x16 O[2];
; #pragma unroll
;         for (int tt = 0; tt < 2; ++tt)
; #pragma unroll
;             for (int r = 0; r < 16; ++r) O[tt][r] = 0.f;
; #pragma unroll
;         for (int et = 0; et < 4; ++et)
; #pragma unroll
;             for (int s2 = 0; s2 < 2; ++s2) {
;                 const bf16x8 sb = pack8(S[et], s2);
; #pragma unroll
;                 for (int tt = 0; tt < 2; ++tt) {
;                     const bf16x8 aq = ld2x64(qb8 + 32 * tt * QS + (32 * et + 16 * s2) * 2);
;                     O[tt] = __builtin_amdgcn_mfma_f32_32x32x16_bf16(aq, sb, O[tt], 0, 0, 0);
;                 }
;             }
;         __syncthreads();
; #pragma unroll
;         for (int pr = 0; pr < 3; ++pr) {
;             const int st = (pr == 2) ? 1 : 0, tt = (pr == 0) ? 0 : 1;
; #pragma unroll
;             for (int s2 = 0; s2 < 2; ++s2) {
;                 const bf16x8 ax = *(const LAS bf16x8*)(frb + (pr * 2 + s2) * 1024);
;                 const LAS unsigned char* vp = vP + (32 * st + 16 * s2) * VS;
;                 const bf16x8 bv = tr8(vp, vp + 8 * VS);
;                 O[tt] = __builtin_amdgcn_mfma_f32_32x32x16_bf16(ax, bv, O[tt], 0, 0, 0);
;             }
;         }
;         __builtin_amdgcn_sched_barrier(0);
; #pragma unroll
;         for (int tt = 0; tt < 2; ++tt)
; #pragma unroll
;             for (int r = 0; r < 16; ++r) ob[(32 * tt + (r & 3) + 8 * (r >> 2)) * OS] = O[tt][r];
;         __builtin_amdgcn_sched_barrier(0);
; #pragma unroll
;         for (int et = 0; et < 4; ++et)
; #pragma unroll
;             for (int rg = 0; rg < 4; ++rg) { const f32x4 dl = *(const LAS f32x4*)&decb[32 * et + 8 * rg];
.LBB0_646:
	v_add_u32_e32 v222, v203, v202
	ds_read2_b64 v[64:67], v222 offset1:2
	v_cvt_pk_bf16_f32 v68, v32, v33
	v_cvt_pk_bf16_f32 v69, v34, v35
	v_cvt_pk_bf16_f32 v70, v36, v37
	v_cvt_pk_bf16_f32 v71, v38, v39
	v_add_u32_e32 v223, 0x2000, v222
	ds_read2_b64 v[228:231], v222 offset0:4 offset1:6
	v_cvt_pk_bf16_f32 v232, v40, v41
	v_cvt_pk_bf16_f32 v233, v42, v43
	s_waitcnt lgkmcnt(1)
	v_mfma_f32_32x32x16_bf16 v[80:95], v[64:67], v[68:71], 0
	ds_read2_b64 v[64:67], v223 offset0:64 offset1:66
	v_cvt_pk_bf16_f32 v234, v44, v45
	v_cvt_pk_bf16_f32 v235, v46, v47
	s_waitcnt lgkmcnt(1)
	s_nop 0
	v_mfma_f32_32x32x16_bf16 v[80:95], v[228:231], v[232:235], v[80:95]
	ds_read2_b64 v[228:231], v223 offset0:68 offset1:70
	s_waitcnt lgkmcnt(1)
	v_mfma_f32_32x32x16_bf16 v[64:79], v[64:67], v[68:71], 0
	s_waitcnt lgkmcnt(0)
	v_mfma_f32_32x32x16_bf16 v[64:79], v[228:231], v[232:235], v[64:79]
	ds_read2_b64 v[228:231], v222 offset0:8 offset1:10
	ds_read2_b64 v[236:239], v223 offset0:72 offset1:74
	ds_read2_b64 v[240:243], v222 offset0:12 offset1:14
	v_cvt_pk_bf16_f32 v232, v16, v17
	v_cvt_pk_bf16_f32 v233, v18, v19
	v_cvt_pk_bf16_f32 v234, v20, v21
	v_cvt_pk_bf16_f32 v235, v22, v23
	s_waitcnt lgkmcnt(2)
	s_nop 0
	v_mfma_f32_32x32x16_bf16 v[80:95], v[228:231], v[232:235], v[80:95]
	ds_read2_b64 v[248:251], v223 offset0:76 offset1:78
	s_waitcnt lgkmcnt(2)
	v_mfma_f32_32x32x16_bf16 v[64:79], v[236:239], v[232:235], v[64:79]
	ds_read2_b64 v[228:231], v222 offset0:16 offset1:18
	v_cvt_pk_bf16_f32 v232, v24, v25
	v_cvt_pk_bf16_f32 v233, v26, v27
	v_cvt_pk_bf16_f32 v234, v28, v29
	v_cvt_pk_bf16_f32 v235, v30, v31
	s_waitcnt lgkmcnt(2)
	s_nop 0
	v_mfma_f32_32x32x16_bf16 v[80:95], v[240:243], v[232:235], v[80:95]
	ds_read2_b64 v[236:239], v223 offset0:80 offset1:82
	s_waitcnt lgkmcnt(2)
	v_mfma_f32_32x32x16_bf16 v[64:79], v[248:251], v[232:235], v[64:79]
	ds_read2_b64 v[240:243], v222 offset0:20 offset1:22
	v_cvt_pk_bf16_f32 v232, v48, v49
	v_cvt_pk_bf16_f32 v233, v50, v51
	v_cvt_pk_bf16_f32 v234, v52, v53
	v_cvt_pk_bf16_f32 v235, v54, v55
	s_waitcnt lgkmcnt(2)
	s_nop 0
	v_mfma_f32_32x32x16_bf16 v[80:95], v[228:231], v[232:235], v[80:95]
	ds_read2_b64 v[248:251], v223 offset0:84 offset1:86
	s_waitcnt lgkmcnt(2)
	v_mfma_f32_32x32x16_bf16 v[64:79], v[236:239], v[232:235], v[64:79]
	ds_read2_b64 v[228:231], v222 offset0:24 offset1:26
	v_cvt_pk_bf16_f32 v232, v56, v57
	v_cvt_pk_bf16_f32 v233, v58, v59
	v_cvt_pk_bf16_f32 v234, v60, v61
	v_cvt_pk_bf16_f32 v235, v62, v63
	s_waitcnt lgkmcnt(2)
	s_nop 0
	v_mfma_f32_32x32x16_bf16 v[80:95], v[240:243], v[232:235], v[80:95]
	ds_read2_b64 v[236:239], v223 offset0:88 offset1:90
	s_waitcnt lgkmcnt(2)
	v_mfma_f32_32x32x16_bf16 v[64:79], v[248:251], v[232:235], v[64:79]
	ds_read2_b64 v[240:243], v222 offset0:28 offset1:30
	v_cvt_pk_bf16_f32 v232, v0, v1
	v_cvt_pk_bf16_f32 v233, v2, v3
	v_cvt_pk_bf16_f32 v234, v4, v5
	v_cvt_pk_bf16_f32 v235, v6, v7
	s_waitcnt lgkmcnt(2)
	s_nop 0
	v_mfma_f32_32x32x16_bf16 v[80:95], v[228:231], v[232:235], v[80:95]
	ds_read2_b64 v[248:251], v223 offset0:92 offset1:94
	s_waitcnt lgkmcnt(2)
	v_mfma_f32_32x32x16_bf16 v[64:79], v[236:239], v[232:235], v[64:79]
	v_cvt_pk_bf16_f32 v232, v8, v9
	v_cvt_pk_bf16_f32 v233, v10, v11
	v_cvt_pk_bf16_f32 v234, v12, v13
	v_cvt_pk_bf16_f32 v235, v14, v15
	s_waitcnt lgkmcnt(1)
	s_nop 0
	v_mfma_f32_32x32x16_bf16 v[80:95], v[240:243], v[232:235], v[80:95]
	s_waitcnt lgkmcnt(0)
	s_barrier
	v_mfma_f32_32x32x16_bf16 v[64:79], v[248:251], v[232:235], v[64:79]
	ds_read_b128 v[228:231], v206
	ds_read_b64_tr_b16 v[232:233], v218
	ds_read_b64_tr_b16 v[234:235], v218 offset:4608
	ds_read_b128 v[236:239], v206 offset:1024
	ds_read_b64_tr_b16 v[240:241], v218 offset:9216
	ds_read_b64_tr_b16 v[242:243], v218 offset:13824
	s_waitcnt lgkmcnt(3)
	v_mfma_f32_32x32x16_bf16 v[80:95], v[228:231], v[232:235], v[80:95]
	s_waitcnt lgkmcnt(0)
	v_mfma_f32_32x32x16_bf16 v[80:95], v[236:239], v[240:243], v[80:95]
	ds_read_b128 v[228:231], v206 offset:2048
	ds_read_b128 v[236:239], v206 offset:3072
	s_waitcnt lgkmcnt(1)
	v_mfma_f32_32x32x16_bf16 v[64:79], v[228:231], v[232:235], v[64:79]
	s_waitcnt lgkmcnt(0)
	v_mfma_f32_32x32x16_bf16 v[64:79], v[236:239], v[240:243], v[64:79]
	ds_read_b128 v[228:231], v206 offset:4096
	ds_read_b64_tr_b16 v[232:233], v218 offset:18432
	ds_read_b64_tr_b16 v[234:235], v218 offset:23040
	ds_read_b128 v[236:239], v206 offset:5120
	ds_read_b64_tr_b16 v[240:241], v218 offset:27648
	ds_read_b64_tr_b16 v[242:243], v218 offset:32256
	s_waitcnt lgkmcnt(3)
	v_mfma_f32_32x32x16_bf16 v[64:79], v[228:231], v[232:235], v[64:79]
	s_waitcnt lgkmcnt(0)
	v_mfma_f32_32x32x16_bf16 v[64:79], v[236:239], v[240:243], v[64:79]
	ds_write_b32 v207, v80
	ds_write_b32 v207, v81 offset:1040
	ds_write_b32 v207, v82 offset:2080
	ds_write_b32 v207, v83 offset:3120
	ds_write_b32 v207, v84 offset:8320
	ds_write_b32 v207, v85 offset:9360
	ds_write_b32 v207, v86 offset:10400
	ds_write_b32 v207, v87 offset:11440
	ds_write_b32 v207, v88 offset:16640
	ds_write_b32 v207, v89 offset:17680
	ds_write_b32 v207, v90 offset:18720
	ds_write_b32 v207, v91 offset:19760
	ds_write_b32 v207, v92 offset:24960
	ds_write_b32 v207, v93 offset:26000
	ds_write_b32 v207, v94 offset:27040
	ds_write_b32 v207, v95 offset:28080
	ds_write_b32 v207, v64 offset:33280
	ds_write_b32 v207, v65 offset:34320
	ds_write_b32 v207, v66 offset:35360
	ds_write_b32 v207, v67 offset:36400
	ds_write_b32 v207, v68 offset:41600
	ds_write_b32 v207, v69 offset:42640
	ds_write_b32 v207, v70 offset:43680
	ds_write_b32 v207, v71 offset:44720
	ds_write_b32 v207, v72 offset:49920
	ds_write_b32 v207, v73 offset:50960
	ds_write_b32 v207, v74 offset:52000
	ds_write_b32 v207, v75 offset:53040
	ds_write_b32 v207, v76 offset:58240
	ds_write_b32 v207, v77 offset:59280
	ds_write_b32 v207, v78 offset:60320
	ds_write_b32 v207, v79 offset:61360
	ds_read_b128 v[64:67], v205
	ds_read_b128 v[68:71], v205 offset:32
	ds_read_b128 v[72:75], v205 offset:64
	ds_read_b128 v[76:79], v205 offset:96
	s_waitcnt vmcnt(11)
; #define LAS __attribute__((address_space(3)))
; __device__ __forceinline__ void gla_unit(LAS unsigned char* lds, const unsigned char* ws, const float* g_onorm, const int b, const int h, const int wv) {
;     ...
; #pragma unroll
;         for (int et = 0; et < 4; ++et)
; #pragma unroll
;             for (int rg = 0; rg < 4; ++rg) { const f32x4 dl = *(const LAS f32x4*)&decb[32 * et + 8 * rg];
; #pragma unroll
;                 for (int x = 0; x < 4; ++x) S[et][4 * rg + x] *= dl[x]; }
; #pragma unroll
;         for (int ks = 0; ks < 4; ++ks) {
;             const LAS unsigned char* vp = vN + 16 * ks * VS;
;             const bf16x8 bv = tr8(vp, vp + 4 * VS);
; #pragma unroll
;             for (int et = 0; et < 4; ++et) {
;                 const LAS unsigned char* kp = keN + 32 * et * 2 + 16 * ks * ES;
;                 const bf16x8 ak = tr8(kp, kp + 4 * ES);
;                 S[et] = __builtin_amdgcn_mfma_f32_32x32x16_bf16(ak, bv, S[et], 0, 0, 0);
;             }
;         }
	v_lshlrev_b32_e32 v246, 16, v176
	s_waitcnt lgkmcnt(3)
	v_pk_mul_f32 v[34:35], v[34:35], v[66:67]
	s_waitcnt lgkmcnt(2)
	v_pk_mul_f32 v[38:39], v[38:39], v[70:71]
	s_waitcnt lgkmcnt(1)
	v_pk_mul_f32 v[42:43], v[42:43], v[74:75]
	s_waitcnt lgkmcnt(0)
	v_pk_mul_f32 v[46:47], v[46:47], v[78:79]
	v_pk_mul_f32 v[44:45], v[44:45], v[76:77]
	v_pk_mul_f32 v[40:41], v[40:41], v[72:73]
	v_pk_mul_f32 v[36:37], v[36:37], v[68:69]
	v_pk_mul_f32 v[32:33], v[32:33], v[64:65]
	ds_read_b128 v[64:67], v205 offset:128
	ds_read_b128 v[68:71], v205 offset:160
	ds_read_b128 v[72:75], v205 offset:192
	ds_read_b128 v[76:79], v205 offset:224
	v_and_b32_e32 v247, 0xffff0000, v176
	s_waitcnt lgkmcnt(3)
	v_pk_mul_f32 v[18:19], v[18:19], v[66:67]
	s_waitcnt lgkmcnt(2)
	v_pk_mul_f32 v[22:23], v[22:23], v[70:71]
	s_waitcnt lgkmcnt(1)
	v_pk_mul_f32 v[26:27], v[26:27], v[74:75]
	s_waitcnt lgkmcnt(0)
	v_pk_mul_f32 v[30:31], v[30:31], v[78:79]
	v_pk_mul_f32 v[28:29], v[28:29], v[76:77]
	v_pk_mul_f32 v[24:25], v[24:25], v[72:73]
	v_pk_mul_f32 v[20:21], v[20:21], v[68:69]
	v_pk_mul_f32 v[16:17], v[16:17], v[64:65]
	ds_read_b128 v[64:67], v205 offset:256
	ds_read_b128 v[68:71], v205 offset:288
	ds_read_b128 v[72:75], v205 offset:320
	ds_read_b128 v[76:79], v205 offset:352
	v_lshlrev_b32_e32 v176, 16, v177
	s_waitcnt lgkmcnt(3)
	v_pk_mul_f32 v[50:51], v[50:51], v[66:67]
	s_waitcnt lgkmcnt(2)
	v_pk_mul_f32 v[54:55], v[54:55], v[70:71]
	s_waitcnt lgkmcnt(1)
	v_pk_mul_f32 v[58:59], v[58:59], v[74:75]
	s_waitcnt lgkmcnt(0)
	v_pk_mul_f32 v[62:63], v[62:63], v[78:79]
	v_pk_mul_f32 v[60:61], v[60:61], v[76:77]
	v_pk_mul_f32 v[56:57], v[56:57], v[72:73]
	v_pk_mul_f32 v[52:53], v[52:53], v[68:69]
	v_pk_mul_f32 v[48:49], v[48:49], v[64:65]
	ds_read_b128 v[64:67], v205 offset:384
	ds_read_b128 v[68:71], v205 offset:416
	ds_read_b128 v[72:75], v205 offset:448
	ds_read_b128 v[76:79], v205 offset:480
	v_and_b32_e32 v177, 0xffff0000, v177
	s_waitcnt lgkmcnt(3)
	v_pk_mul_f32 v[2:3], v[2:3], v[66:67]
	s_waitcnt lgkmcnt(2)
	v_pk_mul_f32 v[6:7], v[6:7], v[70:71]
	v_pk_mul_f32 v[4:5], v[4:5], v[68:69]
	v_pk_mul_f32 v[0:1], v[0:1], v[64:65]
	ds_read_b64_tr_b16 v[64:65], v219
	ds_read_b64_tr_b16 v[66:67], v219 offset:2304
	ds_read_b64_tr_b16 v[68:69], v220
	ds_read_b64_tr_b16 v[70:71], v220 offset:1280
	ds_read_b64_tr_b16 v[80:81], v220 offset:64
	ds_read_b64_tr_b16 v[82:83], v220 offset:1344
	ds_read_b64_tr_b16 v[84:85], v220 offset:128
	ds_read_b64_tr_b16 v[86:87], v220 offset:1408
	ds_read_b64_tr_b16 v[88:89], v220 offset:192
	ds_read_b64_tr_b16 v[90:91], v220 offset:1472
	ds_read_b64_tr_b16 v[92:93], v219 offset:9216
	ds_read_b64_tr_b16 v[94:95], v219 offset:11520
	s_waitcnt lgkmcnt(8)
	v_mfma_f32_32x32x16_bf16 v[32:47], v[68:71], v[64:67], v[32:47]
	ds_read_b64_tr_b16 v[68:69], v220 offset:5120
	ds_read_b64_tr_b16 v[70:71], v220 offset:6400
	v_mul_f32_e64 v14, v14, v78
	v_mul_f32_e64 v15, v15, v79
	v_mul_f32_e64 v10, v10, v74
	v_mul_f32_e64 v11, v11, v75
	v_pk_mul_f32 v[12:13], v[12:13], v[76:77]
	v_pk_mul_f32 v[8:9], v[8:9], v[72:73]
	s_waitcnt lgkmcnt(8)
	v_mfma_f32_32x32x16_bf16 v[16:31], v[80:83], v[64:67], v[16:31]
	ds_read_b64_tr_b16 v[80:81], v220 offset:5184
	ds_read_b64_tr_b16 v[82:83], v220 offset:6464
	s_waitcnt lgkmcnt(8)
	v_mfma_f32_32x32x16_bf16 v[48:63], v[84:87], v[64:67], v[48:63]
	ds_read_b64_tr_b16 v[84:85], v220 offset:5248
	ds_read_b64_tr_b16 v[86:87], v220 offset:6528
	s_waitcnt lgkmcnt(8)
	v_mfma_f32_32x32x16_bf16 v[0:15], v[88:91], v[64:67], v[0:15]
	ds_read_b64_tr_b16 v[88:89], v220 offset:5312
	ds_read_b64_tr_b16 v[90:91], v220 offset:6592
	ds_read_b64_tr_b16 v[64:65], v219 offset:18432
	ds_read_b64_tr_b16 v[66:67], v219 offset:20736
	s_waitcnt lgkmcnt(8)
	v_mfma_f32_32x32x16_bf16 v[32:47], v[68:71], v[92:95], v[32:47]
	ds_read_b64_tr_b16 v[68:69], v220 offset:10240
	ds_read_b64_tr_b16 v[70:71], v220 offset:11520
	s_waitcnt lgkmcnt(8)
	v_mfma_f32_32x32x16_bf16 v[16:31], v[80:83], v[92:95], v[16:31]
	ds_read_b64_tr_b16 v[80:81], v220 offset:10304
	ds_read_b64_tr_b16 v[82:83], v220 offset:11584
	s_waitcnt lgkmcnt(8)
	v_mfma_f32_32x32x16_bf16 v[48:63], v[84:87], v[92:95], v[48:63]
	ds_read_b64_tr_b16 v[84:85], v220 offset:10368
	ds_read_b64_tr_b16 v[86:87], v220 offset:11648
	s_waitcnt lgkmcnt(8)
	v_mfma_f32_32x32x16_bf16 v[0:15], v[88:91], v[92:95], v[0:15]
	ds_read_b64_tr_b16 v[88:89], v220 offset:10432
	ds_read_b64_tr_b16 v[90:91], v220 offset:11712
	ds_read_b64_tr_b16 v[92:93], v219 offset:27648
	ds_read_b64_tr_b16 v[94:95], v219 offset:29952
	s_waitcnt lgkmcnt(8)
	v_mfma_f32_32x32x16_bf16 v[32:47], v[68:71], v[64:67], v[32:47]
	ds_read_b64_tr_b16 v[68:69], v220 offset:15360
	ds_read_b64_tr_b16 v[70:71], v220 offset:16640
	s_waitcnt lgkmcnt(8)
	v_mfma_f32_32x32x16_bf16 v[16:31], v[80:83], v[64:67], v[16:31]
	ds_read_b64_tr_b16 v[80:81], v220 offset:15424
	ds_read_b64_tr_b16 v[82:83], v220 offset:16704
	s_waitcnt lgkmcnt(8)
	v_mfma_f32_32x32x16_bf16 v[48:63], v[84:87], v[64:67], v[48:63]
	ds_read_b64_tr_b16 v[84:85], v220 offset:15488
	ds_read_b64_tr_b16 v[86:87], v220 offset:16768
	s_waitcnt lgkmcnt(8)
	v_mfma_f32_32x32x16_bf16 v[0:15], v[88:91], v[64:67], v[0:15]
	ds_read_b64_tr_b16 v[88:89], v220 offset:15552
	ds_read_b64_tr_b16 v[90:91], v220 offset:16832
	s_waitcnt lgkmcnt(6)
	v_mfma_f32_32x32x16_bf16 v[32:47], v[68:71], v[92:95], v[32:47]
	s_waitcnt lgkmcnt(4)
	v_mfma_f32_32x32x16_bf16 v[16:31], v[80:83], v[92:95], v[16:31]
	s_waitcnt lgkmcnt(2)
	v_mfma_f32_32x32x16_bf16 v[48:63], v[84:87], v[92:95], v[48:63]
	s_waitcnt lgkmcnt(0)
	s_barrier
; #define LAS __attribute__((address_space(3)))
; __device__ __forceinline__ unsigned cvt_pk_bf16(float lo, float hi) { const bf16x2_t r = __builtin_convertvector((f32x2_t){lo, hi}, bf16x2_t); return __builtin_bit_cast(unsigned, r); }
; __device__ __forceinline__ void gla_unit(LAS unsigned char* lds, const unsigned char* ws, const float* g_onorm, const int b, const int h, const int wv) {
;     ...
;                 S[et] = __builtin_amdgcn_mfma_f32_32x32x16_bf16(ak, bv, S[et], 0, 0, 0);
;             }
;         }
;         __syncthreads();
;         {
;             const int t = tid >> 3, g8 = tid & 7;
;             float ov[32]; float ss = 0.f;
; #pragma unroll
;             for (int x = 0; x < 8; ++x) { const f32x4 v = *(const LAS f32x4*)&obuf[t * OS + 32 * g8 + 4 * x]; ov[4 * x] = v[0]; ov[4 * x + 1] = v[1]; ov[4 * x + 2] = v[2]; ov[4 * x + 3] = v[3];
;                 ss += v[0] * v[0] + v[1] * v[1] + v[2] * v[2] + v[3] * v[3]; }
;             ss += __builtin_bit_cast(float, __builtin_amdgcn_ds_swizzle(__builtin_bit_cast(int, ss), (1 << 10) | 0x1F)); ss += __builtin_bit_cast(float, __builtin_amdgcn_ds_swizzle(__builtin_bit_cast(int, ss), (2 << 10) | 0x1F));
;             ss += __builtin_bit_cast(float, __builtin_amdgcn_ds_swizzle(__builtin_bit_cast(int, ss), (4 << 10) | 0x1F));
;             const float rstd = __builtin_amdgcn_rsqf(ss * (1.0f / 256.0f) + EPSV);
;             bf16_t* mp = mix + (t0 + t) * DM + 1024 + h * 256 + 32 * g8;
; #pragma unroll
;             for (int x = 0; x < 4; ++x) {
;                 const u32x4 og = ogr[x];
;                 const f32x4 g0 = *(const LAS f32x4*)&gon[32 * g8 + 8 * x], g1 = *(const LAS f32x4*)&gon[32 * g8 + 8 * x + 4];
;                 const float gg2[8] = {g0[0], g0[1], g0[2], g0[3], g1[0], g1[1], g1[2], g1[3]};
;                 float res[8];
; #pragma unroll
;                 for (int y = 0; y < 4; ++y) { const float a0 = bf_lo(og[y]), a1 = bf_hi(og[y]);
;                     res[2 * y] = ov[8 * x + 2 * y] * rstd * gg2[2 * y] * a0;
;                     res[2 * y + 1] = ov[8 * x + 2 * y + 1] * rstd * gg2[2 * y + 1] * a1; }
;                 u32x4 wv4; wv4[0] = cvt_pk_bf16(res[0], res[1]); wv4[1] = cvt_pk_bf16(res[2], res[3]); wv4[2] = cvt_pk_bf16(res[4], res[5]); wv4[3] = cvt_pk_bf16(res[6], res[7]);
;                 *(u32x4*)(mp + 8 * x) = wv4;
;             }
	v_mfma_f32_32x32x16_bf16 v[0:15], v[88:91], v[92:95], v[0:15]
	ds_read_b128 v[64:67], v221
	ds_read_b128 v[68:71], v221 offset:16
	ds_read_b128 v[72:75], v221 offset:32
	ds_read_b128 v[76:79], v221 offset:48
	s_waitcnt lgkmcnt(3)
	v_mul_f32_e32 v80, v65, v65
	s_waitcnt lgkmcnt(2)
	v_mul_f32_e32 v81, v69, v69
	v_fmac_f32_e32 v80, v64, v64
	v_fmac_f32_e32 v81, v68, v68
	v_fmac_f32_e32 v80, v66, v66
	v_fmac_f32_e32 v81, v70, v70
	v_fmac_f32_e32 v80, v67, v67
	v_fmac_f32_e32 v81, v71, v71
	s_waitcnt lgkmcnt(1)
	v_mov_b32_e32 v82, v73
	s_waitcnt lgkmcnt(0)
	v_mov_b32_e32 v83, v77
	v_add_f32_e32 v84, v80, v81
	v_mov_b32_e32 v80, v72
	v_mov_b32_e32 v81, v76
	v_pk_mul_f32 v[82:83], v[82:83], v[82:83]
	s_nop 0
	v_pk_fma_f32 v[80:81], v[80:81], v[80:81], v[82:83]
	v_mov_b32_e32 v82, v74
	v_mov_b32_e32 v83, v78
	v_pk_fma_f32 v[80:81], v[82:83], v[82:83], v[80:81]
	v_mov_b32_e32 v82, v75
	v_mov_b32_e32 v83, v79
	v_pk_fma_f32 v[80:81], v[82:83], v[82:83], v[80:81]
	s_nop 0
	v_add_f32_e32 v80, v84, v80
	v_add_f32_e32 v92, v80, v81
	ds_read_b128 v[80:83], v221 offset:64
	ds_read_b128 v[84:87], v221 offset:80
	s_waitcnt lgkmcnt(1)
	v_mov_b32_e32 v90, v81
	s_waitcnt lgkmcnt(0)
	v_mov_b32_e32 v91, v85
	v_mov_b32_e32 v88, v80
	v_mov_b32_e32 v89, v84
	v_pk_mul_f32 v[90:91], v[90:91], v[90:91]
	s_nop 0
	v_pk_fma_f32 v[88:89], v[88:89], v[88:89], v[90:91]
	v_mov_b32_e32 v90, v82
	v_mov_b32_e32 v91, v86
	v_pk_fma_f32 v[88:89], v[90:91], v[90:91], v[88:89]
	v_mov_b32_e32 v90, v83
	v_mov_b32_e32 v91, v87
	v_pk_fma_f32 v[88:89], v[90:91], v[90:91], v[88:89]
	s_nop 0
	v_add_f32_e32 v88, v92, v88
	v_add_f32_e32 v227, v88, v89
	ds_read_b128 v[88:91], v221 offset:96
	ds_read_b128 v[92:95], v221 offset:112
	s_waitcnt lgkmcnt(1)
	v_mov_b32_e32 v228, v89
	s_waitcnt lgkmcnt(0)
	v_mov_b32_e32 v229, v93
	v_mov_b32_e32 v200, v88
	v_mov_b32_e32 v201, v92
	v_pk_mul_f32 v[228:229], v[228:229], v[228:229]
	s_nop 0
	v_pk_fma_f32 v[200:201], v[200:201], v[200:201], v[228:229]
	v_mov_b32_e32 v228, v90
	v_mov_b32_e32 v229, v94
	v_pk_fma_f32 v[200:201], v[228:229], v[228:229], v[200:201]
	v_mov_b32_e32 v228, v91
	v_mov_b32_e32 v229, v95
	v_pk_fma_f32 v[200:201], v[228:229], v[228:229], v[200:201]
	ds_read_b128 v[228:231], v208
	ds_read_b128 v[232:235], v208 offset:16
	ds_read_b128 v[236:239], v208 offset:32
	ds_read_b128 v[240:243], v208 offset:48
	v_add_f32_e32 v200, v227, v200
	v_add_f32_e32 v200, v200, v201
	ds_swizzle_b32 v201, v200 offset:swizzle(SWAP,1)
	s_waitcnt lgkmcnt(0)
	v_add_f32_e32 v200, v200, v201
	ds_swizzle_b32 v201, v200 offset:swizzle(SWAP,2)
	s_waitcnt lgkmcnt(0)
	v_add_f32_e32 v200, v200, v201
	ds_swizzle_b32 v201, v200 offset:swizzle(SWAP,4)
	s_waitcnt lgkmcnt(0)
	v_add_f32_e32 v200, v200, v201
	v_fmamk_f32 v200, v200, 0x3b800000, v181
	v_rsq_f32_e32 v244, v200
	v_lshl_add_u64 v[200:201], s[76:77], 0, v[188:189]
	v_pk_mul_f32 v[66:67], v[66:67], v[244:245] op_sel_hi:[1,0]
	s_nop 0
	v_pk_mul_f32 v[66:67], v[230:231], v[66:67]
	v_pk_mul_f32 v[68:69], v[68:69], v[244:245] op_sel_hi:[1,0]
	v_pk_mul_f32 v[64:65], v[64:65], v[244:245] op_sel_hi:[1,0]
	v_pk_mul_f32 v[66:67], v[66:67], v[176:177]
	v_lshlrev_b32_e32 v176, 16, v178
	v_and_b32_e32 v177, 0xffff0000, v178
	v_pk_mul_f32 v[68:69], v[232:233], v[68:69]
	v_pk_mul_f32 v[70:71], v[70:71], v[244:245] op_sel_hi:[1,0]
	v_pk_mul_f32 v[64:65], v[228:229], v[64:65]
	v_pk_mul_f32 v[68:69], v[68:69], v[176:177]
	v_lshlrev_b32_e32 v176, 16, v179
	v_and_b32_e32 v177, 0xffff0000, v179
	v_pk_mul_f32 v[70:71], v[234:235], v[70:71]
	v_pk_mul_f32 v[64:65], v[64:65], v[246:247]
	v_pk_mul_f32 v[70:71], v[70:71], v[176:177]
	v_add_co_u32_e32 v176, vcc, s33, v200
	v_cvt_pk_bf16_f32 v64, v64, v65
	v_cvt_pk_bf16_f32 v65, v66, v67
	v_cvt_pk_bf16_f32 v66, v68, v69
	v_cvt_pk_bf16_f32 v67, v70, v71
	v_addc_co_u32_e32 v177, vcc, 0, v201, vcc
	global_store_dwordx4 v[176:177], v[64:67], off offset:2048
	v_pk_mul_f32 v[68:69], v[74:75], v[244:245] op_sel_hi:[1,0]
	v_pk_mul_f32 v[70:71], v[76:77], v[244:245] op_sel_hi:[1,0]
	v_pk_mul_f32 v[66:67], v[72:73], v[244:245] op_sel_hi:[1,0]
	s_waitcnt vmcnt(9)
; #define LAS __attribute__((address_space(3)))
; __device__ __forceinline__ unsigned cvt_pk_bf16(float lo, float hi) { const bf16x2_t r = __builtin_convertvector((f32x2_t){lo, hi}, bf16x2_t); return __builtin_bit_cast(unsigned, r); }
; __device__ __forceinline__ float bf_lo(unsigned w) { return __uint_as_float(w << 16); }
; __device__ __forceinline__ float bf_hi(unsigned w) { return __uint_as_float(w & 0xffff0000u); }
; __device__ __forceinline__ void gla_unit(LAS unsigned char* lds, const unsigned char* ws, const float* g_onorm, const int b, const int h, const int wv) {
;     ...
;         __syncthreads();
; #pragma unroll
;         for (int i = 0; i < 2; ++i) { const int c = tid + 512 * i, row = c >> 4, cc = (c & 15) * 16;
;             *(LAS u32x4*)(lds + L_Q + row * QS + cc) = qr[par][i]; *(LAS u32x4*)(lds + L_K + row * QS + cc) = kr[par][i]; }
; #pragma unroll
;         for (int i = 0; i < 4; ++i) { const int c = tid + 512 * i; *(LAS u32x4*)(lds + L_V + (c >> 5) * VS + (c & 31) * 16) = vr[par][i]; }
;         if (tid < 32) {
;             const float L2E_ = 1.4426950408889634f;
;             *(LAS f32x4*)&dec[tid * 4] = (f32x4){__builtin_amdgcn_exp2f(dr[0] * L2E_), __builtin_amdgcn_exp2f(dr[1] * L2E_), __builtin_amdgcn_exp2f(dr[2] * L2E_), __builtin_amdgcn_exp2f(dr[3] * L2E_)};
;         }
;     ...
; #pragma unroll
;             for (int x = 0; x < 4; ++x) {
;                 const u32x4 og = ogr[x];
;                 const f32x4 g0 = *(const LAS f32x4*)&gon[32 * g8 + 8 * x], g1 = *(const LAS f32x4*)&gon[32 * g8 + 8 * x + 4];
;                 const float gg2[8] = {g0[0], g0[1], g0[2], g0[3], g1[0], g1[1], g1[2], g1[3]};
;                 float res[8];
; #pragma unroll
;                 for (int y = 0; y < 4; ++y) { const float a0 = bf_lo(og[y]), a1 = bf_hi(og[y]);
;                     res[2 * y] = ov[8 * x + 2 * y] * rstd * gg2[2 * y] * a0;
;                     res[2 * y + 1] = ov[8 * x + 2 * y + 1] * rstd * gg2[2 * y + 1] * a1; }
;                 u32x4 wv4; wv4[0] = cvt_pk_bf16(res[0], res[1]); wv4[1] = cvt_pk_bf16(res[2], res[3]); wv4[2] = cvt_pk_bf16(res[4], res[5]); wv4[3] = cvt_pk_bf16(res[6], res[7]);
;                 *(u32x4*)(mp + 8 * x) = wv4;
;             }
	v_lshlrev_b32_e32 v64, 16, v172
	v_and_b32_e32 v65, 0xffff0000, v172
	v_pk_mul_f32 v[66:67], v[236:237], v[66:67]
	v_pk_mul_f32 v[68:69], v[238:239], v[68:69]
	v_pk_mul_f32 v[64:65], v[66:67], v[64:65]
	v_lshlrev_b32_e32 v66, 16, v173
	v_and_b32_e32 v67, 0xffff0000, v173
	v_pk_mul_f32 v[66:67], v[68:69], v[66:67]
	v_lshlrev_b32_e32 v68, 16, v174
	v_and_b32_e32 v69, 0xffff0000, v174
	v_pk_mul_f32 v[70:71], v[240:241], v[70:71]
	v_pk_mul_f32 v[72:73], v[78:79], v[244:245] op_sel_hi:[1,0]
	v_pk_mul_f32 v[68:69], v[70:71], v[68:69]
	v_lshlrev_b32_e32 v70, 16, v175
	v_and_b32_e32 v71, 0xffff0000, v175
	v_pk_mul_f32 v[72:73], v[242:243], v[72:73]
	v_cvt_pk_bf16_f32 v64, v64, v65
	v_pk_mul_f32 v[70:71], v[72:73], v[70:71]
	v_cvt_pk_bf16_f32 v65, v66, v67
	v_cvt_pk_bf16_f32 v66, v68, v69
	v_cvt_pk_bf16_f32 v67, v70, v71
	global_store_dwordx4 v[176:177], v[64:67], off offset:2064
	ds_read_b128 v[64:67], v208 offset:64
	ds_read_b128 v[68:71], v208 offset:80
	v_pk_mul_f32 v[74:75], v[80:81], v[244:245] op_sel_hi:[1,0]
	v_lshlrev_b32_e32 v72, 16, v168
	v_and_b32_e32 v73, 0xffff0000, v168
	s_waitcnt lgkmcnt(1)
	v_pk_mul_f32 v[64:65], v[64:65], v[74:75]
	v_pk_mul_f32 v[74:75], v[82:83], v[244:245] op_sel_hi:[1,0]
	v_pk_mul_f32 v[64:65], v[64:65], v[72:73]
	v_lshlrev_b32_e32 v72, 16, v169
	v_and_b32_e32 v73, 0xffff0000, v169
	v_pk_mul_f32 v[66:67], v[66:67], v[74:75]
	v_pk_mul_f32 v[74:75], v[84:85], v[244:245] op_sel_hi:[1,0]
	v_pk_mul_f32 v[66:67], v[66:67], v[72:73]
	v_lshlrev_b32_e32 v72, 16, v170
	v_and_b32_e32 v73, 0xffff0000, v170
	s_waitcnt lgkmcnt(0)
	v_pk_mul_f32 v[68:69], v[68:69], v[74:75]
	v_pk_mul_f32 v[74:75], v[86:87], v[244:245] op_sel_hi:[1,0]
	v_pk_mul_f32 v[68:69], v[68:69], v[72:73]
	v_lshlrev_b32_e32 v72, 16, v171
	v_and_b32_e32 v73, 0xffff0000, v171
	v_pk_mul_f32 v[70:71], v[70:71], v[74:75]
	v_cvt_pk_bf16_f32 v64, v64, v65
	v_pk_mul_f32 v[70:71], v[70:71], v[72:73]
	v_cvt_pk_bf16_f32 v65, v66, v67
	v_cvt_pk_bf16_f32 v66, v68, v69
	v_cvt_pk_bf16_f32 v67, v70, v71
	global_store_dwordx4 v[176:177], v[64:67], off offset:2080
	ds_read_b128 v[64:67], v208 offset:96
	ds_read_b128 v[68:71], v208 offset:112
	v_pk_mul_f32 v[74:75], v[88:89], v[244:245] op_sel_hi:[1,0]
	v_lshlrev_b32_e32 v72, 16, v164
	v_and_b32_e32 v73, 0xffff0000, v164
	s_waitcnt lgkmcnt(1)
	v_pk_mul_f32 v[64:65], v[74:75], v[64:65]
	v_pk_mul_f32 v[74:75], v[90:91], v[244:245] op_sel_hi:[1,0]
	v_pk_mul_f32 v[64:65], v[64:65], v[72:73]
	v_lshlrev_b32_e32 v72, 16, v165
	v_and_b32_e32 v73, 0xffff0000, v165
	v_pk_mul_f32 v[66:67], v[74:75], v[66:67]
	v_pk_mul_f32 v[74:75], v[92:93], v[244:245] op_sel_hi:[1,0]
	v_pk_mul_f32 v[66:67], v[66:67], v[72:73]
	v_lshlrev_b32_e32 v72, 16, v166
	v_and_b32_e32 v73, 0xffff0000, v166
	s_waitcnt lgkmcnt(0)
	v_pk_mul_f32 v[68:69], v[74:75], v[68:69]
	v_pk_mul_f32 v[74:75], v[94:95], v[244:245] op_sel_hi:[1,0]
	v_pk_mul_f32 v[68:69], v[68:69], v[72:73]
	v_lshlrev_b32_e32 v72, 16, v167
	v_and_b32_e32 v73, 0xffff0000, v167
	v_pk_mul_f32 v[70:71], v[74:75], v[70:71]
	v_cvt_pk_bf16_f32 v64, v64, v65
	v_pk_mul_f32 v[70:71], v[70:71], v[72:73]
	v_cvt_pk_bf16_f32 v65, v66, v67
	v_cvt_pk_bf16_f32 v66, v68, v69
	v_cvt_pk_bf16_f32 v67, v70, v71
	global_store_dwordx4 v[176:177], v[64:67], off offset:2096
	s_barrier
	s_waitcnt vmcnt(20)
	ds_write_b128 v209, v[132:135]
	ds_write_b128 v209, v[136:139] offset:17408
	ds_write_b128 v210, v[140:143]
	ds_write_b128 v210, v[144:147] offset:17408
	ds_write_b128 v211, v[148:151]
	ds_write_b128 v212, v[152:155]
	ds_write_b128 v213, v[156:159]
	ds_write_b128 v214, v[160:163]
	s_and_saveexec_b64 s[42:43], s[0:1]
	s_cbranch_execz .LBB0_648
	s_waitcnt vmcnt(12)
	v_mul_f32_e32 v64, 0x3fb8aa3b, v124
	v_mul_f32_e32 v65, 0x3fb8aa3b, v125
	v_mul_f32_e32 v66, 0x3fb8aa3b, v126
	v_mul_f32_e32 v67, 0x3fb8aa3b, v127
	v_exp_f32_e32 v64, v64
	v_exp_f32_e32 v65, v65
	v_exp_f32_e32 v66, v66
	v_exp_f32_e32 v67, v67
	ds_write_b128 v226, v[64:67]
